# speedup vs baseline: 1.0041x; 1.0041x over previous
.LBB1_223:
	s_endpgm
	.p2align	8

_Z5k_aggILi0EEvPKDF16_S1_S1_PK15HIP_vector_typeIiLj4EEPKiS7_PKfS1_S9_PfPDF16_S1_S9_SB_SB_:
	s_load_dwordx2 s[6:7], s[0:1], 0x30
	s_load_dwordx2 s[4:5], s[0:1], 0x18
	s_load_dwordx4 s[24:27], s[0:1], 0x20
	s_load_dwordx2 s[30:31], s[0:1], 0x10
	s_load_dwordx4 s[20:23], s[0:1], 0x0
	s_load_dwordx4 s[16:19], s[0:1], 0x58
	s_load_dwordx2 s[28:29], s[0:1], 0x40
	s_and_b32 s36, s2, 7
	s_lshr_b32 s37, s2, 3
	s_mul_i32 s38, s36, 0x61
	s_min_u32 s36, s36, 6
	s_add_i32 s40, s36, s37
	s_add_i32 s40, s40, s38
	s_lshl_b32 s33, s40, 6
	v_lshrrev_b32_e32 v100, 3, v0
	v_and_b32_e32 v101, 7, v0
	v_or_b32_e32 v102, s33, v100
	v_mov_b32_e32 v103, 0
	v_and_b32_e32 v1, 63, v0
	v_lshlrev_b32_e32 v2, 2, v1
	v_or_b32_e32 v16, 0x300, v1
	v_lshlrev_b32_e32 v104, 5, v102
	v_lshl_or_b32 v104, v101, 2, v104
	s_waitcnt lgkmcnt(0)
	v_lshl_add_u64 v[106:107], v[102:103], 4, s[4:5]
	global_load_dwordx3 v[42:44], v[106:107], off
	global_load_dwordx3 v[46:48], v[106:107], off offset:512
	global_load_dword v45, v104, s[26:27]
	global_load_dword v49, v104, s[26:27] offset:1024
	global_load_dword v4, v2, s[6:7]
	global_load_dword v5, v2, s[6:7] offset:256
	global_load_dword v6, v2, s[6:7] offset:512
	global_load_dword v7, v2, s[6:7] offset:768
	global_load_dword v8, v2, s[6:7] offset:1024
	global_load_dword v9, v2, s[6:7] offset:1280
	global_load_dword v10, v2, s[6:7] offset:1536
	global_load_dword v11, v2, s[6:7] offset:1792
	global_load_dword v12, v2, s[6:7] offset:2048
	global_load_dword v13, v2, s[6:7] offset:2304
	global_load_dword v14, v2, s[6:7] offset:2560
	global_load_dword v15, v2, s[6:7] offset:2816
	s_movk_i32 s3, 0x30e
	v_mov_b32_e32 v3, 0
	v_cmp_gt_u32_e32 vcc, s3, v16
	s_waitcnt vmcnt(11)
	v_add_f32_e32 v1, 0, v4
	s_waitcnt vmcnt(10)
	v_add_f32_e32 v1, v1, v5
	s_waitcnt vmcnt(9)
	v_add_f32_e32 v1, v1, v6
	s_waitcnt vmcnt(8)
	v_add_f32_e32 v1, v1, v7
	s_waitcnt vmcnt(7)
	v_add_f32_e32 v1, v1, v8
	s_waitcnt vmcnt(6)
	v_add_f32_e32 v1, v1, v9
	s_waitcnt vmcnt(5)
	v_add_f32_e32 v1, v1, v10
	s_waitcnt vmcnt(4)
	v_add_f32_e32 v1, v1, v11
	s_waitcnt vmcnt(3)
	v_add_f32_e32 v1, v1, v12
	s_waitcnt vmcnt(2)
	v_add_f32_e32 v1, v1, v13
	s_waitcnt vmcnt(1)
	v_add_f32_e32 v1, v1, v14
	s_waitcnt vmcnt(0)
	v_add_f32_e32 v1, v1, v15
	s_and_saveexec_b64 s[8:9], vcc
	s_cbranch_execz .LBB2_2
	v_lshl_add_u64 v[4:5], s[6:7], 0, v[2:3]
	global_load_dword v2, v[4:5], off offset:3072
	s_waitcnt vmcnt(0)
	v_add_f32_e32 v1, v1, v2
.LBB2_2:
	s_or_b64 exec, exec, s[8:9]
	v_mbcnt_lo_u32_b32 v2, -1, 0
	v_mbcnt_hi_u32_b32 v4, -1, v2
	v_and_b32_e32 v2, 64, v4
	v_add_u32_e32 v2, 64, v2
	v_xor_b32_e32 v5, 32, v4
	v_cmp_lt_i32_e32 vcc, v5, v2
	v_xor_b32_e32 v6, 16, v4
	v_cndmask_b32_e32 v5, v4, v5, vcc
	v_lshlrev_b32_e32 v5, 2, v5
	ds_bpermute_b32 v5, v5, v1
	v_cmp_lt_i32_e32 vcc, v6, v2
	s_waitcnt lgkmcnt(0)
	v_add_f32_e32 v1, v1, v5
	v_cndmask_b32_e32 v5, v4, v6, vcc
	v_lshlrev_b32_e32 v5, 2, v5
	ds_bpermute_b32 v5, v5, v1
	v_xor_b32_e32 v6, 8, v4
	v_cmp_lt_i32_e32 vcc, v6, v2
	s_waitcnt lgkmcnt(0)
	v_add_f32_e32 v1, v1, v5
	v_cndmask_b32_e32 v5, v4, v6, vcc
	v_lshlrev_b32_e32 v5, 2, v5
	ds_bpermute_b32 v5, v5, v1
	v_xor_b32_e32 v6, 4, v4
	v_cmp_lt_i32_e32 vcc, v6, v2
	s_waitcnt lgkmcnt(0)
	v_add_f32_e32 v1, v1, v5
	v_cndmask_b32_e32 v5, v4, v6, vcc
	v_lshlrev_b32_e32 v5, 2, v5
	ds_bpermute_b32 v5, v5, v1
	s_waitcnt lgkmcnt(0)
	v_add_f32_e32 v1, v1, v5
	v_xor_b32_e32 v5, 2, v4
	v_cmp_lt_i32_e32 vcc, v5, v2
	s_nop 1
	v_cndmask_b32_e32 v5, v4, v5, vcc
	v_lshlrev_b32_e32 v5, 2, v5
	ds_bpermute_b32 v5, v5, v1
	s_waitcnt lgkmcnt(0)
	v_add_f32_e32 v1, v1, v5
	v_xor_b32_e32 v5, 1, v4
	v_cmp_lt_i32_e32 vcc, v5, v2
	s_nop 1
	v_cndmask_b32_e32 v2, v4, v5, vcc
	v_lshlrev_b32_e32 v2, 2, v2
	ds_bpermute_b32 v2, v2, v1
	s_waitcnt lgkmcnt(0)
	v_add_f32_e32 v1, v1, v2
	s_nop 0
	v_readfirstlane_b32 s6, v1
	s_setprio 2
	v_lshrrev_b32_e32 v1, 3, v0
	v_or_b32_e32 v2, s33, v1
	v_and_b32_e32 v50, 7, v0
	v_cmp_eq_u32_e64 s[8:9], 0, v50
	s_and_saveexec_b64 s[2:3], s[8:9]
	s_cbranch_execz .LBB2_4
	v_lshlrev_b32_e32 v5, 2, v1
	v_add_u32_e32 v5, 0x9c00, v5
	s_waitcnt vmcnt(0)
	ds_write2_b32 v5, v42, v46 offset0:128 offset1:160
.LBB2_4:
	s_or_b64 exec, exec, s[2:3]
	v_mov_b32_e32 v53, 0
	s_waitcnt lgkmcnt(0)
	s_barrier
	v_mov_b32_e32 v2, 0x37a7c5ac
	v_mul_f32_e32 v55, s6, v2
	v_xor_b32_e32 v2, v1, v0
	s_load_dwordx4 s[12:15], s[0:1], 0x68
	s_load_dwordx2 s[26:27], s[0:1], 0x50
	s_load_dwordx2 s[34:35], s[0:1], 0x38
	v_lshlrev_b32_e32 v2, 4, v2
	v_lshlrev_b32_e32 v56, 4, v50
	v_mov_b32_e32 v57, v53
	v_and_b32_e32 v2, 0x70, v2
	v_lshl_add_u64 v[58:59], s[20:21], 0, v[56:57]
	v_lshl_add_u64 v[60:61], s[22:23], 0, v[56:57]
	v_or_b32_e32 v57, 0x8000, v2
	v_bfe_u32 v2, v0, 3, 4
	v_bitop3_b32 v3, v1, v50, 15 bitop3:0x6c
	v_rcp_f32_e32 v54, v55
	v_and_b32_e32 v82, 0x78, v4
	v_lshlrev_b32_e32 v83, 4, v3
	v_bitop3_b32 v3, v50, v2, 8 bitop3:0x36
	v_lshlrev_b32_e32 v84, 4, v3
	v_bitop3_b32 v3, v50, v2, 16 bitop3:0x36
	v_bitop3_b32 v2, v50, v2, 24 bitop3:0x36
	v_lshlrev_b32_e32 v87, 2, v82
	v_lshlrev_b32_e32 v85, 4, v3
	v_lshlrev_b32_e32 v86, 4, v2
	v_or_b32_e32 v88, 4, v87
	v_or_b32_e32 v89, 8, v87
	v_or_b32_e32 v90, 12, v87
	v_or_b32_e32 v91, 16, v87
	v_or_b32_e32 v92, 20, v87
	v_or_b32_e32 v93, 24, v87
	v_lshl_or_b32 v94, v4, 2, 28
	v_mov_b32_e32 v51, v53
	s_mov_b32 s2, 0
	s_mov_b64 s[4:5], -1
	v_mov_b32_e32 v95, 0x1a7a
	s_branch .LBB2_6

.LBB2_86:
	s_branch .LBB2_76
	.p2align	8

_Z5k_aggILi1EEvPKDF16_S1_S1_PK15HIP_vector_typeIiLj4EEPKiS7_PKfS1_S9_PfPDF16_S1_S9_SB_SB_:
	s_load_dwordx2 s[6:7], s[0:1], 0x30
	s_load_dwordx2 s[4:5], s[0:1], 0x18
	s_load_dwordx4 s[20:23], s[0:1], 0x20
	s_load_dwordx2 s[24:25], s[0:1], 0x10
	s_load_dwordx4 s[16:19], s[0:1], 0x0
	s_and_b32 s26, s2, 7
	s_lshr_b32 s27, s2, 3
	s_mul_i32 s28, s26, 0x61
	s_min_u32 s26, s26, 6
	s_add_i32 s30, s26, s27
	s_add_i32 s30, s30, s28
	v_lshrrev_b32_e32 v100, 3, v0
	v_and_b32_e32 v101, 7, v0
	v_lshl_or_b32 v102, s30, 6, v100
	v_mov_b32_e32 v103, 0
	v_and_b32_e32 v1, 63, v0
	v_lshlrev_b32_e32 v2, 2, v1
	v_or_b32_e32 v16, 0x300, v1
	v_lshlrev_b32_e32 v104, 5, v102
	v_lshl_or_b32 v104, v101, 2, v104
	s_waitcnt lgkmcnt(0)
	v_lshl_add_u64 v[106:107], v[102:103], 4, s[4:5]
	global_load_dwordx3 v[42:44], v[106:107], off
	global_load_dwordx3 v[46:48], v[106:107], off offset:512
	global_load_dword v45, v104, s[22:23]
	global_load_dword v49, v104, s[22:23] offset:1024
	global_load_dword v4, v2, s[6:7]
	global_load_dword v5, v2, s[6:7] offset:256
	global_load_dword v6, v2, s[6:7] offset:512
	global_load_dword v7, v2, s[6:7] offset:768
	global_load_dword v8, v2, s[6:7] offset:1024
	global_load_dword v9, v2, s[6:7] offset:1280
	global_load_dword v10, v2, s[6:7] offset:1536
	global_load_dword v11, v2, s[6:7] offset:1792
	global_load_dword v12, v2, s[6:7] offset:2048
	global_load_dword v13, v2, s[6:7] offset:2304
	global_load_dword v14, v2, s[6:7] offset:2560
	global_load_dword v15, v2, s[6:7] offset:2816
	s_movk_i32 s3, 0x30e
	v_mov_b32_e32 v3, 0
	v_cmp_gt_u32_e32 vcc, s3, v16
	s_waitcnt vmcnt(11)
	v_add_f32_e32 v1, 0, v4
	s_waitcnt vmcnt(10)
	v_add_f32_e32 v1, v1, v5
	s_waitcnt vmcnt(9)
	v_add_f32_e32 v1, v1, v6
	s_waitcnt vmcnt(8)
	v_add_f32_e32 v1, v1, v7
	s_waitcnt vmcnt(7)
	v_add_f32_e32 v1, v1, v8
	s_waitcnt vmcnt(6)
	v_add_f32_e32 v1, v1, v9
	s_waitcnt vmcnt(5)
	v_add_f32_e32 v1, v1, v10
	s_waitcnt vmcnt(4)
	v_add_f32_e32 v1, v1, v11
	s_waitcnt vmcnt(3)
	v_add_f32_e32 v1, v1, v12
	s_waitcnt vmcnt(2)
	v_add_f32_e32 v1, v1, v13
	s_waitcnt vmcnt(1)
	v_add_f32_e32 v1, v1, v14
	s_waitcnt vmcnt(0)
	v_add_f32_e32 v1, v1, v15
	s_and_saveexec_b64 s[8:9], vcc
	s_cbranch_execz .LBB3_2
	v_lshl_add_u64 v[4:5], s[6:7], 0, v[2:3]
	global_load_dword v2, v[4:5], off offset:3072
	s_waitcnt vmcnt(0)
	v_add_f32_e32 v1, v1, v2
.LBB3_2:
	s_or_b64 exec, exec, s[8:9]
	v_mbcnt_lo_u32_b32 v2, -1, 0
	v_mbcnt_hi_u32_b32 v4, -1, v2
	v_and_b32_e32 v2, 64, v4
	v_add_u32_e32 v2, 64, v2
	v_xor_b32_e32 v5, 32, v4
	v_cmp_lt_i32_e32 vcc, v5, v2
	v_xor_b32_e32 v6, 16, v4
	v_cndmask_b32_e32 v5, v4, v5, vcc
	v_lshlrev_b32_e32 v5, 2, v5
	ds_bpermute_b32 v5, v5, v1
	v_cmp_lt_i32_e32 vcc, v6, v2
	s_waitcnt lgkmcnt(0)
	v_add_f32_e32 v1, v1, v5
	v_cndmask_b32_e32 v5, v4, v6, vcc
	v_lshlrev_b32_e32 v5, 2, v5
	ds_bpermute_b32 v5, v5, v1
	v_xor_b32_e32 v6, 8, v4
	v_cmp_lt_i32_e32 vcc, v6, v2
	s_waitcnt lgkmcnt(0)
	v_add_f32_e32 v1, v1, v5
	v_cndmask_b32_e32 v5, v4, v6, vcc
	v_lshlrev_b32_e32 v5, 2, v5
	ds_bpermute_b32 v5, v5, v1
	v_xor_b32_e32 v6, 4, v4
	v_cmp_lt_i32_e32 vcc, v6, v2
	s_waitcnt lgkmcnt(0)
	v_add_f32_e32 v1, v1, v5
	v_cndmask_b32_e32 v5, v4, v6, vcc
	v_lshlrev_b32_e32 v5, 2, v5
	ds_bpermute_b32 v5, v5, v1
	v_xor_b32_e32 v6, 2, v4
	v_cmp_lt_i32_e32 vcc, v6, v2
	s_waitcnt lgkmcnt(0)
	v_add_f32_e32 v1, v1, v5
	v_cndmask_b32_e32 v5, v4, v6, vcc
	v_lshlrev_b32_e32 v5, 2, v5
	ds_bpermute_b32 v5, v5, v1
	s_waitcnt lgkmcnt(0)
	v_add_f32_e32 v1, v1, v5
	v_xor_b32_e32 v5, 1, v4
	v_cmp_lt_i32_e32 vcc, v5, v2
	s_nop 1
	v_cndmask_b32_e32 v2, v4, v5, vcc
	v_lshlrev_b32_e32 v2, 2, v2
	ds_bpermute_b32 v2, v2, v1
	s_waitcnt lgkmcnt(0)
	v_add_f32_e32 v1, v1, v2
	s_nop 0
	v_readfirstlane_b32 s6, v1
	s_setprio 2
	v_lshrrev_b32_e32 v1, 3, v0
	v_lshl_or_b32 v2, s30, 6, v1
	v_and_b32_e32 v50, 7, v0
	v_cmp_eq_u32_e64 s[8:9], 0, v50
	s_and_saveexec_b64 s[2:3], s[8:9]
	s_cbranch_execz .LBB3_4
	v_lshlrev_b32_e32 v5, 2, v1
	v_add_u32_e32 v5, 0x9c00, v5
	s_waitcnt vmcnt(0)
	ds_write2_b32 v5, v42, v46 offset0:128 offset1:160
.LBB3_4:
	s_or_b64 exec, exec, s[2:3]
	v_mov_b32_e32 v53, 0
	s_waitcnt lgkmcnt(0)
	s_barrier
	v_mov_b32_e32 v2, 0x37a7c5ac
	v_mul_f32_e32 v55, s6, v2
	v_xor_b32_e32 v2, v1, v0
	v_lshlrev_b32_e32 v2, 4, v2
	s_load_dwordx2 s[22:23], s[0:1], 0x48
	s_load_dwordx4 s[12:15], s[0:1], 0x38
	v_lshlrev_b32_e32 v56, 4, v50
	v_mov_b32_e32 v57, v53
	v_and_b32_e32 v2, 0x70, v2
	v_lshl_add_u64 v[58:59], s[16:17], 0, v[56:57]
	v_lshl_add_u64 v[60:61], s[18:19], 0, v[56:57]
	v_or_b32_e32 v57, 0x8000, v2
	v_bfe_u32 v2, v0, 3, 4
	v_bitop3_b32 v3, v1, v50, 15 bitop3:0x6c
	v_rcp_f32_e32 v54, v55
	v_and_b32_e32 v82, 0x78, v4
	v_lshlrev_b32_e32 v83, 4, v3
	v_bitop3_b32 v3, v50, v2, 8 bitop3:0x36
	v_lshlrev_b32_e32 v84, 4, v3
	v_bitop3_b32 v3, v50, v2, 16 bitop3:0x36
	v_bitop3_b32 v2, v50, v2, 24 bitop3:0x36
	v_lshlrev_b32_e32 v87, 2, v82
	v_lshlrev_b32_e32 v85, 4, v3
	v_lshlrev_b32_e32 v86, 4, v2
	v_or_b32_e32 v88, 4, v87
	v_or_b32_e32 v89, 8, v87
	v_or_b32_e32 v90, 12, v87
	v_or_b32_e32 v91, 16, v87
	v_or_b32_e32 v92, 20, v87
	v_or_b32_e32 v93, 24, v87
	v_lshl_or_b32 v94, v4, 2, 28
	v_mov_b32_e32 v51, v53
	s_mov_b32 s2, 0
	s_mov_b64 s[4:5], -1
	v_mov_b32_e32 v95, 0x1a7a
	s_branch .LBB3_6
